# attention PV: counted lgkmcnt waits per MFMA instead of lgkmcnt(0) per 4-MFMA group
# speedup vs baseline: 1.0082x; 1.0082x over previous
; #define SBAR() __builtin_amdgcn_sched_barrier(0)
; __device__ __forceinline__ void finishSM(f32x16& p0, f32x16& p1, float alpha, float& l_reg, bf16x8& pa0, bf16x8& pa1, bf16x8& pa2, bf16x8& pa3) {
;   for (int r = 0; r < 16; ++r) p1[r] = __builtin_amdgcn_exp2f(p1[r]);
;   float ps = 0; for (int r = 0; r < 16; ++r) ps += p0[r]; for (int r = 0; r < 16; ++r) ps += p1[r];
;   { auto rr = __builtin_amdgcn_permlane32_swap(__float_as_uint(ps), __float_as_uint(ps), false, false);
;     ps = __uint_as_float(rr[0]) + __uint_as_float(rr[1]); }
;   l_reg = l_reg * alpha + ps;
;     ...
;   PK4(p0, 0, pa0); PK4(p0, 8, pa1); PK4(p1, 0, pa2); PK4(p1, 8, pa3);
;     ...
; }
; template <bool HALF> __device__ __forceinline__ void qkt(f32x16& p0, f32x16& p1, const char* Ks, const bf16x8* qr, int r32, int hi, int koff) {
;   p0 = f32x16{}; p1 = f32x16{};
;   for (int d0 = 0; d0 < (HALF ? 4 : 8); ++d0) { int cb = (d0 * 16 + hi * 8) * 2 + koff;
;     bf16x8 b0 = *reinterpret_cast<const bf16x8*>(Ks + KSWZ(r32, cb));
;     bf16x8 b1 = *reinterpret_cast<const bf16x8*>(Ks + KSWZ(32 + r32, cb));
;     p0 = __builtin_amdgcn_mfma_f32_32x32x16_bf16(b0, qr[d0], p0, 0, 0, 0);
;     p1 = __builtin_amdgcn_mfma_f32_32x32x16_bf16(b1, qr[d0], p1, 0, 0, 0); }
; template <int D0> __device__ __forceinline__ void pv_one(f32x16& od, int vb, bf16x8 pa0, bf16x8 pa1, bf16x8 pa2, bf16x8 pa3) {
;   const s16x4 l0 = tr_read<v_rd_off(D0, 0, 0)>(vb), h0 = tr_read<v_rd_off(D0, 0, 1)>(vb), l1 = tr_read<v_rd_off(D0, 1, 0)>(vb), h1 = tr_read<v_rd_off(D0, 1, 1)>(vb);
;   const s16x4 l2 = tr_read<v_rd_off(D0, 2, 0)>(vb), h2 = tr_read<v_rd_off(D0, 2, 1)>(vb), l3 = tr_read<v_rd_off(D0, 3, 0)>(vb), h3 = tr_read<v_rd_off(D0, 3, 1)>(vb);
;   asm volatile("s_waitcnt lgkmcnt(0)" ::: "memory"); SBAR();
;     ...
;   od = __builtin_amdgcn_mfma_f32_32x32x16_bf16(pa0, PK(l0, h0), od, 0, 0, 0);
;   od = __builtin_amdgcn_mfma_f32_32x32x16_bf16(pa1, PK(l1, h1), od, 0, 0, 0);
;   od = __builtin_amdgcn_mfma_f32_32x32x16_bf16(pa2, PK(l2, h2), od, 0, 0, 0);
;   od = __builtin_amdgcn_mfma_f32_32x32x16_bf16(pa3, PK(l3, h3), od, 0, 0, 0);
;     ...
; }
; __device__ __forceinline__ void pv_d0(f32x16* o, int vb, bf16x8 pa0, bf16x8 pa1, bf16x8 pa2, bf16x8 pa3) {
;   pv_one<0>(o[0], vb, pa0, pa1, pa2, pa3); pv_one<1>(o[1], vb, pa0, pa1, pa2, pa3); pv_one<2>(o[2], vb, pa0, pa1, pa2, pa3); pv_one<3>(o[3], vb, pa0, pa1, pa2, pa3);
.LBB0_425:
	ds_read_b128 v[64:67], v209 offset:49152
	ds_read_b128 v[68:71], v209 offset:57344
	ds_read_b128 v[190:193], v221 offset:49152
	ds_read_b128 v[228:231], v221 offset:57344
	v_add_f32_e32 v162, 0, v163
	v_add_f32_e32 v162, v177, v162
	s_waitcnt lgkmcnt(3)
	v_mfma_f32_32x32x16_bf16 v[80:95], v[64:67], v[118:121], 0
	v_add_f32_e32 v162, v164, v162
	v_add_f32_e32 v162, v188, v162
	v_add_f32_e32 v162, v176, v162
	v_add_f32_e32 v162, v189, v162
	v_add_f32_e32 v162, v165, v162
	v_add_f32_e32 v162, v175, v162
	v_add_f32_e32 v162, v166, v162
	s_waitcnt lgkmcnt(2)
	v_mfma_f32_32x32x16_bf16 v[64:79], v[68:71], v[118:121], 0
	v_add_f32_e32 v162, v173, v162
	v_add_f32_e32 v162, v167, v162
	v_add_f32_e32 v162, v174, v162
	v_exp_f32_e32 v160, v160
	v_add_f32_e32 v162, v168, v162
	v_exp_f32_e32 v161, v161
	v_add_f32_e32 v162, v171, v162
	s_waitcnt lgkmcnt(1)
	v_mfma_f32_32x32x16_bf16 v[80:95], v[190:193], v[126:129], v[80:95]
	v_exp_f32_e32 v158, v158
	v_add_f32_e32 v162, v169, v162
	v_exp_f32_e32 v159, v159
	v_add_f32_e32 v162, v172, v162
	v_exp_f32_e32 v154, v154
	v_add_f32_e32 v162, v160, v162
	v_exp_f32_e32 v155, v155
	s_waitcnt lgkmcnt(0)
	v_mfma_f32_32x32x16_bf16 v[64:79], v[228:231], v[126:129], v[64:79]
	ds_read_b128 v[190:193], v222 offset:49152
	ds_read_b128 v[228:231], v222 offset:57344
	v_add_f32_e32 v162, v161, v162
	v_exp_f32_e32 v150, v150
	v_add_f32_e32 v162, v158, v162
	v_exp_f32_e32 v151, v151
	v_add_f32_e32 v162, v159, v162
	v_exp_f32_e32 v148, v148
	s_waitcnt lgkmcnt(1)
	v_mfma_f32_32x32x16_bf16 v[80:95], v[190:193], v[122:125], v[80:95]
	v_add_f32_e32 v162, v154, v162
	v_exp_f32_e32 v149, v149
	v_add_f32_e32 v162, v155, v162
	v_exp_f32_e32 v156, v156
	v_add_f32_e32 v162, v150, v162
	v_exp_f32_e32 v157, v157
	v_add_f32_e32 v162, v151, v162
	s_waitcnt lgkmcnt(0)
	v_mfma_f32_32x32x16_bf16 v[64:79], v[228:231], v[122:125], v[64:79]
	ds_read_b128 v[190:193], v210 offset:49152
	ds_read_b128 v[228:231], v210 offset:57344
	v_exp_f32_e32 v152, v152
	v_add_f32_e32 v162, v148, v162
	v_exp_f32_e32 v153, v153
	v_add_f32_e32 v162, v149, v162
	v_exp_f32_e32 v146, v146
	v_add_f32_e32 v162, v156, v162
	s_waitcnt lgkmcnt(1)
	v_mfma_f32_32x32x16_bf16 v[80:95], v[190:193], v[114:117], v[80:95]
	v_exp_f32_e32 v147, v147
	v_add_f32_e32 v162, v157, v162
	v_add_f32_e32 v162, v152, v162
	v_add_f32_e32 v162, v153, v162
	v_add_f32_e32 v162, v146, v162
	v_add_f32_e32 v227, v147, v162
	s_waitcnt lgkmcnt(0)
	v_mfma_f32_32x32x16_bf16 v[64:79], v[228:231], v[114:117], v[64:79]
	ds_read_b128 v[190:193], v211 offset:49152
	ds_read_b128 v[228:231], v211 offset:57344
	s_waitcnt lgkmcnt(1)
	v_mfma_f32_32x32x16_bf16 v[80:95], v[190:193], v[110:113], v[80:95]
	s_waitcnt lgkmcnt(0)
	v_mfma_f32_32x32x16_bf16 v[64:79], v[228:231], v[110:113], v[64:79]
	ds_read_b128 v[190:193], v223 offset:49152
	ds_read_b128 v[228:231], v223 offset:57344
	s_waitcnt lgkmcnt(1)
	v_mfma_f32_32x32x16_bf16 v[80:95], v[190:193], v[106:109], v[80:95]
	s_waitcnt lgkmcnt(0)
	v_mfma_f32_32x32x16_bf16 v[64:79], v[228:231], v[106:109], v[64:79]
	ds_read_b128 v[190:193], v225 offset:49152
	ds_read_b128 v[228:231], v225 offset:57344
	s_waitcnt lgkmcnt(1)
	v_mfma_f32_32x32x16_bf16 v[80:95], v[190:193], v[102:105], v[80:95]
	s_waitcnt lgkmcnt(0)
	v_mfma_f32_32x32x16_bf16 v[64:79], v[228:231], v[102:105], v[64:79]
	ds_read_b128 v[190:193], v224 offset:49152
	ds_read_b128 v[228:231], v224 offset:57344
	v_cvt_pk_bf16_f32 v162, v163, v177
	v_cvt_pk_bf16_f32 v163, v164, v188
	v_cvt_pk_bf16_f32 v164, v176, v189
	v_cvt_pk_bf16_f32 v165, v165, v175
	v_cvt_pk_bf16_f32 v166, v166, v173
	v_cvt_pk_bf16_f32 v167, v167, v174
	s_waitcnt lgkmcnt(1)
	v_mfma_f32_32x32x16_bf16 v[80:95], v[190:193], v[98:101], v[80:95]
	v_permlane32_swap_b32_e32 v162, v164
	v_cvt_pk_bf16_f32 v168, v168, v171
	v_cvt_pk_bf16_f32 v169, v169, v172
	v_cvt_pk_bf16_f32 v172, v160, v161
	v_cvt_pk_bf16_f32 v173, v158, v159
	v_cvt_pk_bf16_f32 v174, v154, v155
	s_waitcnt lgkmcnt(0)
	v_mfma_f32_32x32x16_bf16 v[64:79], v[228:231], v[98:101], v[64:79]
	v_mov_b32_e32 v228, v227
	s_nop 1
	v_permlane32_swap_b32_e32 v227, v228
	v_cvt_pk_bf16_f32 v175, v150, v151
	v_cvt_pk_bf16_f32 v230, v148, v149
	v_cvt_pk_bf16_f32 v231, v156, v157
	v_cvt_pk_bf16_f32 v232, v152, v153
	v_cvt_pk_bf16_f32 v233, v146, v147
	v_permlane32_swap_b32_e32 v163, v165
	v_permlane32_swap_b32_e32 v166, v168
	v_permlane32_swap_b32_e32 v167, v169
	v_permlane32_swap_b32_e32 v172, v174
	v_permlane32_swap_b32_e32 v173, v175
	v_permlane32_swap_b32_e32 v230, v232
	v_permlane32_swap_b32_e32 v231, v233
	ds_read_b64_tr_b16 v[234:235], v204 offset:0
	ds_read_b64_tr_b16 v[236:237], v204 offset:0x800
	ds_read_b64_tr_b16 v[238:239], v204 offset:0x1000
	ds_read_b64_tr_b16 v[240:241], v204 offset:0x1800
	ds_read_b64_tr_b16 v[242:243], v204 offset:0x2000
	ds_read_b64_tr_b16 v[244:245], v204 offset:0x2800
	ds_read_b64_tr_b16 v[246:247], v204 offset:0x3000
	ds_read_b64_tr_b16 v[248:249], v204 offset:0x3800
	s_nop 0
	s_waitcnt lgkmcnt(6)
	v_mfma_f32_32x32x16_bf16 v[0:15], v[162:165], v[234:237], v[0:15]
	ds_read_b64_tr_b16 v[234:235], v204 offset:0x200
	ds_read_b64_tr_b16 v[236:237], v204 offset:0xa00
	s_waitcnt lgkmcnt(6)
	v_mfma_f32_32x32x16_bf16 v[0:15], v[166:169], v[238:241], v[0:15]
	ds_read_b64_tr_b16 v[238:239], v204 offset:0x1200
	ds_read_b64_tr_b16 v[240:241], v204 offset:0x1a00
	s_waitcnt lgkmcnt(6)
	v_mfma_f32_32x32x16_bf16 v[0:15], v[172:175], v[242:245], v[0:15]
	ds_read_b64_tr_b16 v[242:243], v204 offset:0x2200
	ds_read_b64_tr_b16 v[244:245], v204 offset:0x2a00
	s_waitcnt lgkmcnt(6)
; #define SBAR() __builtin_amdgcn_sched_barrier(0)
; __device__ __forceinline__ void partialSM(f32x16& p0, f32x16& p1, float& m_reg, float& mn, float& alpha) {
;     ...
;   float pmax = p0[0]; for (int r = 1; r < 16; ++r) pmax = fmaxf(pmax, p0[r]); for (int r = 0; r < 16; ++r) pmax = fmaxf(pmax, p1[r]);
;   { auto rr = __builtin_amdgcn_permlane32_swap(__float_as_uint(pmax), __float_as_uint(pmax), false, false);
;     pmax = fmaxf(__uint_as_float(rr[0]), __uint_as_float(rr[1])); }
;   if (__builtin_expect(__all(pmax - m_reg <= THR / SCALE), 1)) { mn = m_reg; alpha = 1.f; }
;   else { mn = fmaxf(m_reg, pmax); alpha = __builtin_amdgcn_exp2f((m_reg - mn) * C); m_reg = mn; }
; template <int D0> __device__ __forceinline__ void pv_one(f32x16& od, int vb, bf16x8 pa0, bf16x8 pa1, bf16x8 pa2, bf16x8 pa3) {
;   const s16x4 l0 = tr_read<v_rd_off(D0, 0, 0)>(vb), h0 = tr_read<v_rd_off(D0, 0, 1)>(vb), l1 = tr_read<v_rd_off(D0, 1, 0)>(vb), h1 = tr_read<v_rd_off(D0, 1, 1)>(vb);
;   const s16x4 l2 = tr_read<v_rd_off(D0, 2, 0)>(vb), h2 = tr_read<v_rd_off(D0, 2, 1)>(vb), l3 = tr_read<v_rd_off(D0, 3, 0)>(vb), h3 = tr_read<v_rd_off(D0, 3, 1)>(vb);
;   asm volatile("s_waitcnt lgkmcnt(0)" ::: "memory"); SBAR();
;     ...
;   od = __builtin_amdgcn_mfma_f32_32x32x16_bf16(pa0, PK(l0, h0), od, 0, 0, 0);
;   od = __builtin_amdgcn_mfma_f32_32x32x16_bf16(pa1, PK(l1, h1), od, 0, 0, 0);
;   od = __builtin_amdgcn_mfma_f32_32x32x16_bf16(pa2, PK(l2, h2), od, 0, 0, 0);
;   od = __builtin_amdgcn_mfma_f32_32x32x16_bf16(pa3, PK(l3, h3), od, 0, 0, 0);
;     ...
; }
; __device__ __forceinline__ void pv_d0(f32x16* o, int vb, bf16x8 pa0, bf16x8 pa1, bf16x8 pa2, bf16x8 pa3) {
;   pv_one<0>(o[0], vb, pa0, pa1, pa2, pa3); pv_one<1>(o[1], vb, pa0, pa1, pa2, pa3); pv_one<2>(o[2], vb, pa0, pa1, pa2, pa3); pv_one<3>(o[3], vb, pa0, pa1, pa2, pa3);
	v_mfma_f32_32x32x16_bf16 v[0:15], v[230:233], v[246:249], v[0:15]
	ds_read_b64_tr_b16 v[246:247], v204 offset:0x3200
	ds_read_b64_tr_b16 v[248:249], v204 offset:0x3a00
	s_waitcnt lgkmcnt(6)
	v_mfma_f32_32x32x16_bf16 v[48:63], v[162:165], v[234:237], v[48:63]
	ds_read_b64_tr_b16 v[234:235], v204 offset:0x400
	ds_read_b64_tr_b16 v[236:237], v204 offset:0xc00
	s_waitcnt lgkmcnt(6)
	v_mfma_f32_32x32x16_bf16 v[48:63], v[166:169], v[238:241], v[48:63]
	ds_read_b64_tr_b16 v[238:239], v204 offset:0x1400
	ds_read_b64_tr_b16 v[240:241], v204 offset:0x1c00
	s_waitcnt lgkmcnt(6)
	v_mfma_f32_32x32x16_bf16 v[48:63], v[172:175], v[242:245], v[48:63]
	ds_read_b64_tr_b16 v[242:243], v204 offset:0x2400
	ds_read_b64_tr_b16 v[244:245], v204 offset:0x2c00
	s_waitcnt lgkmcnt(6)
	v_mfma_f32_32x32x16_bf16 v[48:63], v[230:233], v[246:249], v[48:63]
	ds_read_b64_tr_b16 v[246:247], v204 offset:0x3400
	ds_read_b64_tr_b16 v[248:249], v204 offset:0x3c00
	s_waitcnt lgkmcnt(6)
	v_mfma_f32_32x32x16_bf16 v[32:47], v[162:165], v[234:237], v[32:47]
	ds_read_b64_tr_b16 v[234:235], v204 offset:0x600
	ds_read_b64_tr_b16 v[236:237], v204 offset:0xe00
	s_waitcnt lgkmcnt(6)
	v_mfma_f32_32x32x16_bf16 v[32:47], v[166:169], v[238:241], v[32:47]
	ds_read_b64_tr_b16 v[238:239], v204 offset:0x1600
	ds_read_b64_tr_b16 v[240:241], v204 offset:0x1e00
	s_waitcnt lgkmcnt(6)
	v_mfma_f32_32x32x16_bf16 v[32:47], v[172:175], v[242:245], v[32:47]
	ds_read_b64_tr_b16 v[242:243], v204 offset:0x2600
	ds_read_b64_tr_b16 v[244:245], v204 offset:0x2e00
	s_waitcnt lgkmcnt(6)
	v_mfma_f32_32x32x16_bf16 v[32:47], v[230:233], v[246:249], v[32:47]
	ds_read_b64_tr_b16 v[246:247], v204 offset:0x3600
	ds_read_b64_tr_b16 v[248:249], v204 offset:0x3e00
	s_waitcnt lgkmcnt(6)
	v_mfma_f32_32x32x16_bf16 v[16:31], v[162:165], v[234:237], v[16:31]
	v_max_f32_e32 v162, v81, v81
	v_max_f32_e32 v163, v80, v80
	v_max_f32_e32 v162, v163, v162
	v_max3_f32 v162, v162, v82, v83
	v_max3_f32 v162, v162, v84, v85
	v_max3_f32 v162, v162, v86, v87
	v_max3_f32 v162, v162, v88, v89
	v_max3_f32 v162, v162, v90, v91
	v_max3_f32 v162, v162, v92, v93
	s_waitcnt lgkmcnt(4)
	v_mfma_f32_32x32x16_bf16 v[16:31], v[166:169], v[238:241], v[16:31]
	v_max3_f32 v162, v162, v94, v95
	v_max3_f32 v162, v162, v64, v65
	v_max3_f32 v162, v162, v66, v67
	v_max3_f32 v162, v162, v68, v69
	v_max3_f32 v162, v162, v70, v71
	v_max3_f32 v162, v162, v72, v73
	v_max3_f32 v162, v162, v74, v75
	v_max3_f32 v162, v162, v76, v77
	s_waitcnt lgkmcnt(2)
	v_mfma_f32_32x32x16_bf16 v[16:31], v[172:175], v[242:245], v[16:31]
	v_max3_f32 v162, v162, v78, v79
	v_mov_b32_e32 v163, v162
	s_nop 1
	v_permlane32_swap_b32_e32 v162, v163
	v_max_f32_e32 v163, v163, v163
	v_max_f32_e32 v162, v162, v162
	v_max_f32_e32 v162, v162, v163
	v_sub_f32_e32 v163, v162, v170
	v_cmp_ge_f32_e32 vcc, s87, v163
	v_max_f32_e32 v163, v170, v170
	v_max_f32_e32 v162, v163, v162
	s_waitcnt lgkmcnt(0)
	v_mfma_f32_32x32x16_bf16 v[16:31], v[230:233], v[246:249], v[16:31]
	v_sub_f32_e32 v163, v170, v162
	v_mul_f32_e32 v163, 0x3e0293ee, v163
	v_exp_f32_e32 v163, v163
	s_cmp_eq_u64 vcc, exec
	s_cselect_b64 s[42:43], -1, 0
	s_waitcnt vmcnt(0)
	s_barrier
	s_add_i32 m0, s52, 0x4000
	s_nop 0
	global_load_lds_dwordx4 v130, s[48:49]
	s_add_i32 m0, s52, 0x4400
	s_nop 0
	global_load_lds_dwordx4 v131, s[48:49]
	s_add_i32 m0, s53, 0x0
	s_nop 0
	global_load_lds_dwordx4 v132, s[50:51]
	s_add_i32 m0, s53, 0x400
	s_nop 0
	global_load_lds_dwordx4 v133, s[50:51]
	s_add_u32 s48, s48, 0x18000
	s_addc_u32 s49, s49, 0
	s_add_u32 s50, s50, 0xc0000
	s_addc_u32 s51, s51, 0
	v_cndmask_b32_e64 v229, v163, 1.0, s[42:43]
	v_cmp_gt_f32_e32 vcc, 1.0, v229
	s_cbranch_vccz .LBB0_429
	s_and_saveexec_b64 s[6:7], s[40:41]
	ds_write_b32 v201, v229 offset:128
	s_or_b64 exec, exec, s[6:7]
	s_waitcnt lgkmcnt(0)
	v_add_u32_e32 v163, v200, v96
	ds_read_b128 v[164:167], v163 offset:224
	ds_read_b128 v[172:175], v163 offset:192
	ds_read_b128 v[230:233], v163 offset:160
	ds_read_b128 v[234:237], v163 offset:128
	s_waitcnt lgkmcnt(3)
	v_pk_mul_f32 v[12:13], v[12:13], v[164:165]
	s_waitcnt lgkmcnt(2)
	v_pk_mul_f32 v[8:9], v[8:9], v[172:173]
	s_waitcnt lgkmcnt(1)
	v_pk_mul_f32 v[4:5], v[4:5], v[230:231]
	v_pk_mul_f32 v[14:15], v[14:15], v[166:167]
	v_pk_mul_f32 v[10:11], v[10:11], v[174:175]
	v_pk_mul_f32 v[6:7], v[6:7], v[232:233]
	s_waitcnt lgkmcnt(0)
	v_pk_mul_f32 v[2:3], v[2:3], v[236:237]
	v_pk_mul_f32 v[0:1], v[0:1], v[234:235]
	v_pk_mul_f32 v[60:61], v[60:61], v[164:165]
	v_pk_mul_f32 v[56:57], v[56:57], v[172:173]
	v_pk_mul_f32 v[52:53], v[52:53], v[230:231]
	v_pk_mul_f32 v[62:63], v[62:63], v[166:167]
	v_pk_mul_f32 v[58:59], v[58:59], v[174:175]
	v_pk_mul_f32 v[54:55], v[54:55], v[232:233]
	v_pk_mul_f32 v[50:51], v[50:51], v[236:237]
	v_pk_mul_f32 v[48:49], v[48:49], v[234:235]
	v_pk_mul_f32 v[44:45], v[44:45], v[164:165]
	v_pk_mul_f32 v[40:41], v[40:41], v[172:173]
	v_pk_mul_f32 v[36:37], v[36:37], v[230:231]
	v_pk_mul_f32 v[46:47], v[46:47], v[166:167]
	v_pk_mul_f32 v[42:43], v[42:43], v[174:175]
	v_pk_mul_f32 v[38:39], v[38:39], v[232:233]
	v_pk_mul_f32 v[34:35], v[34:35], v[236:237]
	v_pk_mul_f32 v[32:33], v[32:33], v[234:235]
	v_pk_mul_f32 v[28:29], v[28:29], v[164:165]
	v_pk_mul_f32 v[24:25], v[24:25], v[172:173]
	v_pk_mul_f32 v[20:21], v[20:21], v[230:231]
	v_pk_mul_f32 v[30:31], v[30:31], v[166:167]
	v_pk_mul_f32 v[26:27], v[26:27], v[174:175]
	v_pk_mul_f32 v[22:23], v[22:23], v[232:233]
	v_pk_mul_f32 v[18:19], v[18:19], v[236:237]
	v_pk_mul_f32 v[16:17], v[16:17], v[234:235]

; #define SBAR() __builtin_amdgcn_sched_barrier(0)
; __device__ __forceinline__ void partialSM(f32x16& p0, f32x16& p1, float& m_reg, float& mn, float& alpha) {
;     ...
;   float pmax = p0[0]; for (int r = 1; r < 16; ++r) pmax = fmaxf(pmax, p0[r]); for (int r = 0; r < 16; ++r) pmax = fmaxf(pmax, p1[r]);
;   { auto rr = __builtin_amdgcn_permlane32_swap(__float_as_uint(pmax), __float_as_uint(pmax), false, false);
;     pmax = fmaxf(__uint_as_float(rr[0]), __uint_as_float(rr[1])); }
;   if (__builtin_expect(__all(pmax - m_reg <= THR / SCALE), 1)) { mn = m_reg; alpha = 1.f; }
;   else { mn = fmaxf(m_reg, pmax); alpha = __builtin_amdgcn_exp2f((m_reg - mn) * C); m_reg = mn; }
; template <int D0> __device__ __forceinline__ void pv_one(f32x16& od, int vb, bf16x8 pa0, bf16x8 pa1, bf16x8 pa2, bf16x8 pa3) {
;   const s16x4 l0 = tr_read<v_rd_off(D0, 0, 0)>(vb), h0 = tr_read<v_rd_off(D0, 0, 1)>(vb), l1 = tr_read<v_rd_off(D0, 1, 0)>(vb), h1 = tr_read<v_rd_off(D0, 1, 1)>(vb);
;   const s16x4 l2 = tr_read<v_rd_off(D0, 2, 0)>(vb), h2 = tr_read<v_rd_off(D0, 2, 1)>(vb), l3 = tr_read<v_rd_off(D0, 3, 0)>(vb), h3 = tr_read<v_rd_off(D0, 3, 1)>(vb);
;   asm volatile("s_waitcnt lgkmcnt(0)" ::: "memory"); SBAR();
;     ...
;   od = __builtin_amdgcn_mfma_f32_32x32x16_bf16(pa0, PK(l0, h0), od, 0, 0, 0);
;   od = __builtin_amdgcn_mfma_f32_32x32x16_bf16(pa1, PK(l1, h1), od, 0, 0, 0);
;   od = __builtin_amdgcn_mfma_f32_32x32x16_bf16(pa2, PK(l2, h2), od, 0, 0, 0);
;   od = __builtin_amdgcn_mfma_f32_32x32x16_bf16(pa3, PK(l3, h3), od, 0, 0, 0);
;     ...
; }
; __device__ __forceinline__ void pv_d0(f32x16* o, int vb, bf16x8 pa0, bf16x8 pa1, bf16x8 pa2, bf16x8 pa3) {
;   pv_one<0>(o[0], vb, pa0, pa1, pa2, pa3); pv_one<1>(o[1], vb, pa0, pa1, pa2, pa3); pv_one<2>(o[2], vb, pa0, pa1, pa2, pa3); pv_one<3>(o[3], vb, pa0, pa1, pa2, pa3);
.LBB0_431:
	ds_read_b64_tr_b16 v[188:189], v203 offset:0
	ds_read_b64_tr_b16 v[190:191], v203 offset:0x800
	ds_read_b64_tr_b16 v[192:193], v203 offset:0x1000
	ds_read_b64_tr_b16 v[194:195], v203 offset:0x1800
	ds_read_b64_tr_b16 v[212:213], v203 offset:0x2000
	ds_read_b64_tr_b16 v[214:215], v203 offset:0x2800
	ds_read_b64_tr_b16 v[234:235], v203 offset:0x3000
	ds_read_b64_tr_b16 v[236:237], v203 offset:0x3800
	s_nop 0
	s_waitcnt lgkmcnt(6)
	v_mfma_f32_32x32x16_bf16 v[0:15], v[162:165], v[188:191], v[0:15]
	ds_read_b64_tr_b16 v[188:189], v203 offset:0x200
	ds_read_b64_tr_b16 v[190:191], v203 offset:0xa00
	s_waitcnt lgkmcnt(6)
	v_mfma_f32_32x32x16_bf16 v[0:15], v[166:169], v[192:195], v[0:15]
	ds_read_b64_tr_b16 v[192:193], v203 offset:0x1200
	ds_read_b64_tr_b16 v[194:195], v203 offset:0x1a00
	s_waitcnt lgkmcnt(6)
	v_mfma_f32_32x32x16_bf16 v[0:15], v[170:173], v[212:215], v[0:15]
	ds_read_b64_tr_b16 v[212:213], v203 offset:0x2200
	ds_read_b64_tr_b16 v[214:215], v203 offset:0x2a00
	s_waitcnt lgkmcnt(6)
	v_mfma_f32_32x32x16_bf16 v[0:15], v[174:177], v[234:237], v[0:15]
	ds_read_b64_tr_b16 v[234:235], v203 offset:0x3200
	ds_read_b64_tr_b16 v[236:237], v203 offset:0x3a00
	s_waitcnt lgkmcnt(6)
	v_mfma_f32_32x32x16_bf16 v[48:63], v[162:165], v[188:191], v[48:63]
	ds_read_b64_tr_b16 v[188:189], v203 offset:0x400
	ds_read_b64_tr_b16 v[190:191], v203 offset:0xc00
	s_waitcnt lgkmcnt(6)
	v_mfma_f32_32x32x16_bf16 v[48:63], v[166:169], v[192:195], v[48:63]
	ds_read_b64_tr_b16 v[192:193], v203 offset:0x1400
	ds_read_b64_tr_b16 v[194:195], v203 offset:0x1c00
	s_waitcnt lgkmcnt(6)
	v_mfma_f32_32x32x16_bf16 v[48:63], v[170:173], v[212:215], v[48:63]
	ds_read_b64_tr_b16 v[212:213], v203 offset:0x2400
	ds_read_b64_tr_b16 v[214:215], v203 offset:0x2c00
	s_waitcnt lgkmcnt(6)
	v_mfma_f32_32x32x16_bf16 v[48:63], v[174:177], v[234:237], v[48:63]
	ds_read_b64_tr_b16 v[234:235], v203 offset:0x3400
	ds_read_b64_tr_b16 v[236:237], v203 offset:0x3c00
	s_waitcnt lgkmcnt(6)
	v_mfma_f32_32x32x16_bf16 v[32:47], v[162:165], v[188:191], v[32:47]
	ds_read_b64_tr_b16 v[188:189], v203 offset:0x600
	ds_read_b64_tr_b16 v[190:191], v203 offset:0xe00
	s_waitcnt lgkmcnt(6)
	v_mfma_f32_32x32x16_bf16 v[32:47], v[166:169], v[192:195], v[32:47]
	ds_read_b64_tr_b16 v[192:193], v203 offset:0x1600
	ds_read_b64_tr_b16 v[194:195], v203 offset:0x1e00
	s_waitcnt lgkmcnt(6)
	v_mfma_f32_32x32x16_bf16 v[32:47], v[170:173], v[212:215], v[32:47]
	ds_read_b64_tr_b16 v[212:213], v203 offset:0x2600
	ds_read_b64_tr_b16 v[214:215], v203 offset:0x2e00
	s_waitcnt lgkmcnt(6)
	v_mfma_f32_32x32x16_bf16 v[32:47], v[174:177], v[234:237], v[32:47]
	ds_read_b64_tr_b16 v[234:235], v203 offset:0x3600
	ds_read_b64_tr_b16 v[236:237], v203 offset:0x3e00
	s_waitcnt lgkmcnt(6)
	v_mfma_f32_32x32x16_bf16 v[16:31], v[162:165], v[188:191], v[16:31]
	v_max_f32_e32 v162, v81, v81
	v_max_f32_e32 v163, v80, v80
	v_max_f32_e32 v162, v163, v162
	v_max3_f32 v162, v162, v82, v83
	v_max3_f32 v162, v162, v84, v85
	v_max3_f32 v162, v162, v86, v87
	v_max3_f32 v162, v162, v88, v89
	v_max3_f32 v162, v162, v90, v91
	v_max3_f32 v162, v162, v92, v93
	s_waitcnt lgkmcnt(4)
	v_mfma_f32_32x32x16_bf16 v[16:31], v[166:169], v[192:195], v[16:31]
	v_max3_f32 v162, v162, v94, v95
	v_max3_f32 v162, v162, v64, v65
	v_max3_f32 v162, v162, v66, v67
	v_max3_f32 v162, v162, v68, v69
	v_max3_f32 v162, v162, v70, v71
	v_max3_f32 v162, v162, v72, v73
	v_max3_f32 v162, v162, v74, v75
	v_max3_f32 v162, v162, v76, v77
	s_waitcnt lgkmcnt(2)
	v_mfma_f32_32x32x16_bf16 v[16:31], v[170:173], v[212:215], v[16:31]
	v_max3_f32 v162, v162, v78, v79
	v_mov_b32_e32 v163, v162
	s_nop 1
	v_permlane32_swap_b32_e32 v162, v163
	v_max_f32_e32 v163, v163, v163
	v_max_f32_e32 v162, v162, v162
	v_max_f32_e32 v162, v162, v163
	v_sub_f32_e32 v163, v162, v230
	v_cmp_ge_f32_e32 vcc, s87, v163
	v_max_f32_e32 v163, v230, v230
	v_max_f32_e32 v163, v163, v162
	s_waitcnt lgkmcnt(0)
	v_mfma_f32_32x32x16_bf16 v[16:31], v[174:177], v[234:237], v[16:31]
	v_sub_f32_e32 v162, v230, v163
	v_mul_f32_e32 v162, 0x3e0293ee, v162
	v_exp_f32_e32 v162, v162
	s_cmp_eq_u64 vcc, exec
	s_cselect_b64 s[42:43], -1, 0
	s_waitcnt vmcnt(0)
	s_barrier
	s_add_i32 m0, s52, 0x0
	s_nop 0
	global_load_lds_dwordx4 v130, s[48:49]
	s_add_i32 m0, s52, 0x400
	s_nop 0
	global_load_lds_dwordx4 v131, s[48:49]
	s_add_i32 m0, s53, 0x4000
	s_nop 0
	global_load_lds_dwordx4 v132, s[50:51]
	s_add_i32 m0, s53, 0x4400
	s_nop 0
	global_load_lds_dwordx4 v133, s[50:51]
	s_add_u32 s48, s48, 0x18000
	s_addc_u32 s49, s49, 0
	s_add_u32 s50, s50, 0xc0000
	s_addc_u32 s51, s51, 0
	v_cndmask_b32_e64 v162, v162, 1.0, s[42:43]
	v_cmp_gt_f32_e32 vcc, 1.0, v162
	s_cbranch_vccz .LBB0_435
	s_and_saveexec_b64 s[6:7], s[40:41]
	ds_write_b32 v201, v162 offset:128
	s_or_b64 exec, exec, s[6:7]
	s_waitcnt lgkmcnt(0)
	v_add_u32_e32 v158, v200, v96
	ds_read_b128 v[146:149], v158 offset:224
	ds_read_b128 v[150:153], v158 offset:192
	ds_read_b128 v[154:157], v158 offset:160
	ds_read_b128 v[158:161], v158 offset:128
	s_waitcnt lgkmcnt(3)
	v_pk_mul_f32 v[12:13], v[12:13], v[146:147]
	s_waitcnt lgkmcnt(2)
	v_pk_mul_f32 v[8:9], v[8:9], v[150:151]
	s_waitcnt lgkmcnt(1)
	v_pk_mul_f32 v[4:5], v[4:5], v[154:155]
	v_pk_mul_f32 v[14:15], v[14:15], v[148:149]
	v_pk_mul_f32 v[10:11], v[10:11], v[152:153]
	v_pk_mul_f32 v[6:7], v[6:7], v[156:157]
	s_waitcnt lgkmcnt(0)
	v_pk_mul_f32 v[2:3], v[2:3], v[160:161]
	v_pk_mul_f32 v[0:1], v[0:1], v[158:159]
	v_pk_mul_f32 v[60:61], v[60:61], v[146:147]
	v_pk_mul_f32 v[56:57], v[56:57], v[150:151]
	v_pk_mul_f32 v[52:53], v[52:53], v[154:155]
	v_pk_mul_f32 v[62:63], v[62:63], v[148:149]
	v_pk_mul_f32 v[58:59], v[58:59], v[152:153]
	v_pk_mul_f32 v[54:55], v[54:55], v[156:157]
	v_pk_mul_f32 v[50:51], v[50:51], v[160:161]
	v_pk_mul_f32 v[48:49], v[48:49], v[158:159]
	v_pk_mul_f32 v[44:45], v[44:45], v[146:147]
	v_pk_mul_f32 v[40:41], v[40:41], v[150:151]
	v_pk_mul_f32 v[36:37], v[36:37], v[154:155]
	v_pk_mul_f32 v[46:47], v[46:47], v[148:149]
	v_pk_mul_f32 v[42:43], v[42:43], v[152:153]
	v_pk_mul_f32 v[38:39], v[38:39], v[156:157]
	v_pk_mul_f32 v[34:35], v[34:35], v[160:161]
	v_pk_mul_f32 v[32:33], v[32:33], v[158:159]
	v_pk_mul_f32 v[28:29], v[28:29], v[146:147]
	v_pk_mul_f32 v[24:25], v[24:25], v[150:151]
	v_pk_mul_f32 v[20:21], v[20:21], v[154:155]
	v_pk_mul_f32 v[30:31], v[30:31], v[148:149]
	v_pk_mul_f32 v[26:27], v[26:27], v[152:153]
	v_pk_mul_f32 v[22:23], v[22:23], v[156:157]
	v_pk_mul_f32 v[18:19], v[18:19], v[160:161]
	v_pk_mul_f32 v[16:17], v[16:17], v[158:159]

; #define SBAR() __builtin_amdgcn_sched_barrier(0)
; __device__ __forceinline__ void finishSM(f32x16& p0, f32x16& p1, float alpha, float& l_reg, bf16x8& pa0, bf16x8& pa1, bf16x8& pa2, bf16x8& pa3) {
;   for (int r = 0; r < 16; ++r) p1[r] = __builtin_amdgcn_exp2f(p1[r]);
;   float ps = 0; for (int r = 0; r < 16; ++r) ps += p0[r]; for (int r = 0; r < 16; ++r) ps += p1[r];
;   { auto rr = __builtin_amdgcn_permlane32_swap(__float_as_uint(ps), __float_as_uint(ps), false, false);
;     ps = __uint_as_float(rr[0]) + __uint_as_float(rr[1]); }
;   l_reg = l_reg * alpha + ps;
;     ...
;   PK4(p0, 0, pa0); PK4(p0, 8, pa1); PK4(p1, 0, pa2); PK4(p1, 8, pa3);
;     ...
; }
; template <bool HALF> __device__ __forceinline__ void qkt(f32x16& p0, f32x16& p1, const char* Ks, const bf16x8* qr, int r32, int hi, int koff) {
;   p0 = f32x16{}; p1 = f32x16{};
;   for (int d0 = 0; d0 < (HALF ? 4 : 8); ++d0) { int cb = (d0 * 16 + hi * 8) * 2 + koff;
;     bf16x8 b0 = *reinterpret_cast<const bf16x8*>(Ks + KSWZ(r32, cb));
;     bf16x8 b1 = *reinterpret_cast<const bf16x8*>(Ks + KSWZ(32 + r32, cb));
;     p0 = __builtin_amdgcn_mfma_f32_32x32x16_bf16(b0, qr[d0], p0, 0, 0, 0);
;     p1 = __builtin_amdgcn_mfma_f32_32x32x16_bf16(b1, qr[d0], p1, 0, 0, 0); }
; template <int D0> __device__ __forceinline__ void pv_one(f32x16& od, int vb, bf16x8 pa0, bf16x8 pa1, bf16x8 pa2, bf16x8 pa3) {
;   const s16x4 l0 = tr_read<v_rd_off(D0, 0, 0)>(vb), h0 = tr_read<v_rd_off(D0, 0, 1)>(vb), l1 = tr_read<v_rd_off(D0, 1, 0)>(vb), h1 = tr_read<v_rd_off(D0, 1, 1)>(vb);
;   const s16x4 l2 = tr_read<v_rd_off(D0, 2, 0)>(vb), h2 = tr_read<v_rd_off(D0, 2, 1)>(vb), l3 = tr_read<v_rd_off(D0, 3, 0)>(vb), h3 = tr_read<v_rd_off(D0, 3, 1)>(vb);
;   asm volatile("s_waitcnt lgkmcnt(0)" ::: "memory"); SBAR();
;     ...
;   od = __builtin_amdgcn_mfma_f32_32x32x16_bf16(pa0, PK(l0, h0), od, 0, 0, 0);
;   od = __builtin_amdgcn_mfma_f32_32x32x16_bf16(pa1, PK(l1, h1), od, 0, 0, 0);
;   od = __builtin_amdgcn_mfma_f32_32x32x16_bf16(pa2, PK(l2, h2), od, 0, 0, 0);
;   od = __builtin_amdgcn_mfma_f32_32x32x16_bf16(pa3, PK(l3, h3), od, 0, 0, 0);
;     ...
; }
; __device__ __forceinline__ void pv_d0(f32x16* o, int vb, bf16x8 pa0, bf16x8 pa1, bf16x8 pa2, bf16x8 pa3) {
;   pv_one<0>(o[0], vb, pa0, pa1, pa2, pa3); pv_one<1>(o[1], vb, pa0, pa1, pa2, pa3); pv_one<2>(o[2], vb, pa0, pa1, pa2, pa3); pv_one<3>(o[3], vb, pa0, pa1, pa2, pa3);
.LBB0_454:
	ds_read_b128 v[64:67], v192 offset:49152
	ds_read_b128 v[68:71], v192 offset:57344
	v_add_f32_e32 v146, 0, v147
	v_add_f32_e32 v146, v160, v146
	v_add_f32_e32 v146, v148, v146
	s_waitcnt lgkmcnt(1)
	v_mfma_f32_32x32x16_bf16 v[80:95], v[64:67], v[98:101], 0
	v_add_f32_e32 v146, v161, v146
	v_add_f32_e32 v146, v149, v146
	ds_read_b128 v[172:175], v193 offset:49152
	ds_read_b128 v[198:201], v193 offset:57344
	v_add_f32_e32 v146, v170, v146
	v_add_f32_e32 v146, v159, v146
	v_add_f32_e32 v146, v171, v146
	v_add_f32_e32 v146, v151, v146
	s_waitcnt lgkmcnt(2)
	v_mfma_f32_32x32x16_bf16 v[64:79], v[68:71], v[98:101], 0
	v_add_f32_e32 v146, v155, v146
	v_add_f32_e32 v146, v152, v146
	v_add_f32_e32 v146, v156, v146
	v_exp_f32_e32 v144, v144
	v_add_f32_e32 v146, v153, v146
	v_exp_f32_e32 v145, v145
	v_add_f32_e32 v146, v157, v146
	s_waitcnt lgkmcnt(1)
	v_mfma_f32_32x32x16_bf16 v[80:95], v[172:175], v[106:109], v[80:95]
	v_exp_f32_e32 v142, v142
	v_add_f32_e32 v146, v154, v146
	v_exp_f32_e32 v143, v143
	v_add_f32_e32 v146, v158, v146
	v_exp_f32_e32 v138, v138
	v_add_f32_e32 v146, v144, v146
	v_exp_f32_e32 v139, v139
	s_waitcnt lgkmcnt(0)
	v_mfma_f32_32x32x16_bf16 v[64:79], v[198:201], v[106:109], v[64:79]
	ds_read_b128 v[172:175], v195 offset:49152
	ds_read_b128 v[198:201], v195 offset:57344
	v_add_f32_e32 v146, v145, v146
	v_exp_f32_e32 v134, v134
	v_add_f32_e32 v146, v142, v146
	v_exp_f32_e32 v135, v135
	v_add_f32_e32 v146, v143, v146
	v_exp_f32_e32 v132, v132
	s_waitcnt lgkmcnt(1)
	v_mfma_f32_32x32x16_bf16 v[80:95], v[172:175], v[110:113], v[80:95]
	v_add_f32_e32 v146, v138, v146
	v_exp_f32_e32 v133, v133
	v_add_f32_e32 v146, v139, v146
	v_exp_f32_e32 v140, v140
	v_add_f32_e32 v146, v134, v146
	v_exp_f32_e32 v141, v141
	v_add_f32_e32 v146, v135, v146
	s_waitcnt lgkmcnt(0)
	v_mfma_f32_32x32x16_bf16 v[64:79], v[198:201], v[110:113], v[64:79]
	ds_read_b128 v[172:175], v194 offset:49152
	ds_read_b128 v[198:201], v194 offset:57344
	v_exp_f32_e32 v136, v136
	v_add_f32_e32 v146, v132, v146
	v_exp_f32_e32 v137, v137
	v_add_f32_e32 v146, v133, v146
	v_exp_f32_e32 v130, v130
	v_add_f32_e32 v146, v140, v146
	s_waitcnt lgkmcnt(1)
	v_mfma_f32_32x32x16_bf16 v[80:95], v[172:175], v[102:105], v[80:95]
	v_exp_f32_e32 v131, v131
	v_add_f32_e32 v146, v141, v146
	v_add_f32_e32 v146, v136, v146
	v_add_f32_e32 v146, v137, v146
	v_add_f32_e32 v146, v130, v146
	s_waitcnt lgkmcnt(0)
	v_mfma_f32_32x32x16_bf16 v[64:79], v[198:201], v[102:105], v[64:79]
	v_add_f32_e32 v198, v131, v146
	v_mov_b32_e32 v199, v198
	v_cvt_pk_bf16_f32 v146, v147, v160
	v_cvt_pk_bf16_f32 v147, v148, v161
	v_cvt_pk_bf16_f32 v148, v149, v170
	v_cvt_pk_bf16_f32 v149, v159, v171
	v_cvt_pk_bf16_f32 v200, v151, v155
	v_cvt_pk_bf16_f32 v201, v152, v156
	v_cvt_pk_bf16_f32 v202, v153, v157
	s_nop 1
	v_permlane32_swap_b32_e32 v198, v199
	v_permlane32_swap_b32_e32 v146, v148
	v_cvt_pk_bf16_f32 v203, v154, v158
	v_permlane32_swap_b32_e32 v200, v202
	v_cvt_pk_bf16_f32 v152, v144, v145
	v_cvt_pk_bf16_f32 v153, v142, v143
	v_cvt_pk_bf16_f32 v154, v138, v139
	v_cvt_pk_bf16_f32 v155, v134, v135
	v_cvt_pk_bf16_f32 v156, v132, v133
	v_cvt_pk_bf16_f32 v157, v140, v141
	v_cvt_pk_bf16_f32 v158, v136, v137
	v_cvt_pk_bf16_f32 v159, v130, v131
	v_permlane32_swap_b32_e32 v147, v149
	v_permlane32_swap_b32_e32 v201, v203
	v_permlane32_swap_b32_e32 v152, v154
	v_permlane32_swap_b32_e32 v153, v155
	v_permlane32_swap_b32_e32 v156, v158
	v_permlane32_swap_b32_e32 v157, v159
	ds_read_b64_tr_b16 v[204:205], v187 offset:0
	ds_read_b64_tr_b16 v[206:207], v187 offset:0x800
	ds_read_b64_tr_b16 v[208:209], v187 offset:0x1000
	ds_read_b64_tr_b16 v[210:211], v187 offset:0x1800
	ds_read_b64_tr_b16 v[212:213], v187 offset:0x2000
	ds_read_b64_tr_b16 v[214:215], v187 offset:0x2800
	ds_read_b64_tr_b16 v[222:223], v187 offset:0x3000
	ds_read_b64_tr_b16 v[224:225], v187 offset:0x3800
	s_nop 0
	s_waitcnt lgkmcnt(6)
	v_mfma_f32_32x32x16_bf16 v[0:15], v[146:149], v[204:207], v[0:15]
	ds_read_b64_tr_b16 v[204:205], v187 offset:0x200
	ds_read_b64_tr_b16 v[206:207], v187 offset:0xa00
	s_waitcnt lgkmcnt(6)
	v_mfma_f32_32x32x16_bf16 v[0:15], v[200:203], v[208:211], v[0:15]
	ds_read_b64_tr_b16 v[208:209], v187 offset:0x1200
	ds_read_b64_tr_b16 v[210:211], v187 offset:0x1a00
	s_waitcnt lgkmcnt(6)
	v_mfma_f32_32x32x16_bf16 v[0:15], v[152:155], v[212:215], v[0:15]
	ds_read_b64_tr_b16 v[212:213], v187 offset:0x2200
	ds_read_b64_tr_b16 v[214:215], v187 offset:0x2a00
	s_waitcnt lgkmcnt(6)
	v_mfma_f32_32x32x16_bf16 v[0:15], v[156:159], v[222:225], v[0:15]
	ds_read_b64_tr_b16 v[222:223], v187 offset:0x3200
	ds_read_b64_tr_b16 v[224:225], v187 offset:0x3a00
	s_waitcnt lgkmcnt(6)
	v_mfma_f32_32x32x16_bf16 v[48:63], v[146:149], v[204:207], v[48:63]
	ds_read_b64_tr_b16 v[204:205], v187 offset:0x400
	ds_read_b64_tr_b16 v[206:207], v187 offset:0xc00
	s_waitcnt lgkmcnt(6)
	v_mfma_f32_32x32x16_bf16 v[48:63], v[200:203], v[208:211], v[48:63]
	ds_read_b64_tr_b16 v[208:209], v187 offset:0x1400
	ds_read_b64_tr_b16 v[210:211], v187 offset:0x1c00
	s_waitcnt lgkmcnt(6)
; #define SBAR() __builtin_amdgcn_sched_barrier(0)
; __device__ __forceinline__ void partialSM(f32x16& p0, f32x16& p1, float& m_reg, float& mn, float& alpha) {
;     ...
;   float pmax = p0[0]; for (int r = 1; r < 16; ++r) pmax = fmaxf(pmax, p0[r]); for (int r = 0; r < 16; ++r) pmax = fmaxf(pmax, p1[r]);
;   { auto rr = __builtin_amdgcn_permlane32_swap(__float_as_uint(pmax), __float_as_uint(pmax), false, false);
;     pmax = fmaxf(__uint_as_float(rr[0]), __uint_as_float(rr[1])); }
;   if (__builtin_expect(__all(pmax - m_reg <= THR / SCALE), 1)) { mn = m_reg; alpha = 1.f; }
;   else { mn = fmaxf(m_reg, pmax); alpha = __builtin_amdgcn_exp2f((m_reg - mn) * C); m_reg = mn; }
; template <int D0> __device__ __forceinline__ void pv_one(f32x16& od, int vb, bf16x8 pa0, bf16x8 pa1, bf16x8 pa2, bf16x8 pa3) {
;   const s16x4 l0 = tr_read<v_rd_off(D0, 0, 0)>(vb), h0 = tr_read<v_rd_off(D0, 0, 1)>(vb), l1 = tr_read<v_rd_off(D0, 1, 0)>(vb), h1 = tr_read<v_rd_off(D0, 1, 1)>(vb);
;   const s16x4 l2 = tr_read<v_rd_off(D0, 2, 0)>(vb), h2 = tr_read<v_rd_off(D0, 2, 1)>(vb), l3 = tr_read<v_rd_off(D0, 3, 0)>(vb), h3 = tr_read<v_rd_off(D0, 3, 1)>(vb);
;   asm volatile("s_waitcnt lgkmcnt(0)" ::: "memory"); SBAR();
;     ...
;   od = __builtin_amdgcn_mfma_f32_32x32x16_bf16(pa0, PK(l0, h0), od, 0, 0, 0);
;   od = __builtin_amdgcn_mfma_f32_32x32x16_bf16(pa1, PK(l1, h1), od, 0, 0, 0);
;   od = __builtin_amdgcn_mfma_f32_32x32x16_bf16(pa2, PK(l2, h2), od, 0, 0, 0);
;   od = __builtin_amdgcn_mfma_f32_32x32x16_bf16(pa3, PK(l3, h3), od, 0, 0, 0);
;     ...
; }
; __device__ __forceinline__ void pv_d0(f32x16* o, int vb, bf16x8 pa0, bf16x8 pa1, bf16x8 pa2, bf16x8 pa3) {
;   pv_one<0>(o[0], vb, pa0, pa1, pa2, pa3); pv_one<1>(o[1], vb, pa0, pa1, pa2, pa3); pv_one<2>(o[2], vb, pa0, pa1, pa2, pa3); pv_one<3>(o[3], vb, pa0, pa1, pa2, pa3);
	v_mfma_f32_32x32x16_bf16 v[48:63], v[152:155], v[212:215], v[48:63]
	ds_read_b64_tr_b16 v[212:213], v187 offset:0x2400
	ds_read_b64_tr_b16 v[214:215], v187 offset:0x2c00
	s_waitcnt lgkmcnt(6)
	v_mfma_f32_32x32x16_bf16 v[48:63], v[156:159], v[222:225], v[48:63]
	ds_read_b64_tr_b16 v[222:223], v187 offset:0x3400
	ds_read_b64_tr_b16 v[224:225], v187 offset:0x3c00
	s_waitcnt lgkmcnt(6)
	v_mfma_f32_32x32x16_bf16 v[32:47], v[146:149], v[204:207], v[32:47]
	ds_read_b64_tr_b16 v[204:205], v187 offset:0x600
	ds_read_b64_tr_b16 v[206:207], v187 offset:0xe00
	s_waitcnt lgkmcnt(6)
	v_mfma_f32_32x32x16_bf16 v[32:47], v[200:203], v[208:211], v[32:47]
	ds_read_b64_tr_b16 v[208:209], v187 offset:0x1600
	ds_read_b64_tr_b16 v[210:211], v187 offset:0x1e00
	s_waitcnt lgkmcnt(6)
	v_mfma_f32_32x32x16_bf16 v[32:47], v[152:155], v[212:215], v[32:47]
	ds_read_b64_tr_b16 v[212:213], v187 offset:0x2600
	ds_read_b64_tr_b16 v[214:215], v187 offset:0x2e00
	s_waitcnt lgkmcnt(6)
	v_mfma_f32_32x32x16_bf16 v[32:47], v[156:159], v[222:225], v[32:47]
	ds_read_b64_tr_b16 v[222:223], v187 offset:0x3600
	ds_read_b64_tr_b16 v[224:225], v187 offset:0x3e00
	s_waitcnt lgkmcnt(6)
	v_mfma_f32_32x32x16_bf16 v[16:31], v[146:149], v[204:207], v[16:31]
	v_max_f32_e32 v146, v81, v81
	v_max_f32_e32 v147, v80, v80
	v_max_f32_e32 v146, v147, v146
	v_max3_f32 v146, v146, v82, v83
	v_max3_f32 v146, v146, v84, v85
	v_max3_f32 v146, v146, v86, v87
	v_max3_f32 v146, v146, v88, v89
	v_max3_f32 v146, v146, v90, v91
	v_max3_f32 v146, v146, v92, v93
	s_waitcnt lgkmcnt(4)
	v_mfma_f32_32x32x16_bf16 v[16:31], v[200:203], v[208:211], v[16:31]
	v_max3_f32 v146, v146, v94, v95
	v_max3_f32 v146, v146, v64, v65
	v_max3_f32 v146, v146, v66, v67
	v_max3_f32 v146, v146, v68, v69
	v_max3_f32 v146, v146, v70, v71
	v_max3_f32 v146, v146, v72, v73
	v_max3_f32 v146, v146, v74, v75
	v_max3_f32 v146, v146, v76, v77
	s_waitcnt lgkmcnt(2)
	v_mfma_f32_32x32x16_bf16 v[16:31], v[152:155], v[212:215], v[16:31]
	v_max3_f32 v146, v146, v78, v79
	v_mov_b32_e32 v147, v146
	s_nop 1
	v_permlane32_swap_b32_e32 v146, v147
	v_max_f32_e32 v147, v147, v147
	v_max_f32_e32 v146, v146, v146
	v_max_f32_e32 v146, v146, v147
	v_sub_f32_e32 v147, v146, v150
	v_cmp_ge_f32_e32 vcc, s87, v147
	v_max_f32_e32 v147, v150, v150
	v_max_f32_e32 v146, v147, v146
	s_waitcnt lgkmcnt(0)
	v_mfma_f32_32x32x16_bf16 v[16:31], v[156:159], v[222:225], v[16:31]
	v_sub_f32_e32 v147, v150, v146
	v_mul_f32_e32 v147, 0x3e0293ee, v147
	v_exp_f32_e32 v147, v147
	s_cmp_eq_u64 vcc, exec
	s_cselect_b64 s[42:43], -1, 0
	s_waitcnt vmcnt(0)
	s_barrier
	s_add_i32 m0, s52, 0x4000
	s_nop 0
	global_load_lds_dwordx4 v232, s[48:49]
	s_add_i32 m0, s52, 0x4400
	s_nop 0
	global_load_lds_dwordx4 v233, s[48:49]
	s_add_i32 m0, s53, 0x0
	s_nop 0
	global_load_lds_dwordx4 v234, s[50:51]
	s_add_i32 m0, s53, 0x400
	s_nop 0
	global_load_lds_dwordx4 v235, s[50:51]
	s_add_u32 s48, s48, 0x18000
	s_addc_u32 s49, s49, 0
	s_add_u32 s50, s50, 0xc0000
	s_addc_u32 s51, s51, 0
	v_cndmask_b32_e64 v200, v147, 1.0, s[42:43]
	v_cmp_gt_f32_e32 vcc, 1.0, v200
	s_cbranch_vccz .LBB0_458
	s_and_saveexec_b64 s[6:7], s[40:41]
	ds_write_b32 v184, v200 offset:128
	s_or_b64 exec, exec, s[6:7]
	s_waitcnt lgkmcnt(0)
	v_add_u32_e32 v147, v183, v96
	ds_read_b128 v[152:155], v147 offset:224
	ds_read_b128 v[156:159], v147 offset:192
	ds_read_b128 v[202:205], v147 offset:160
	ds_read_b128 v[206:209], v147 offset:128
	s_waitcnt lgkmcnt(3)
	v_pk_mul_f32 v[12:13], v[12:13], v[152:153]
	s_waitcnt lgkmcnt(2)
	v_pk_mul_f32 v[8:9], v[8:9], v[156:157]
	s_waitcnt lgkmcnt(1)
	v_pk_mul_f32 v[4:5], v[4:5], v[202:203]
	v_pk_mul_f32 v[14:15], v[14:15], v[154:155]
	v_pk_mul_f32 v[10:11], v[10:11], v[158:159]
	v_pk_mul_f32 v[6:7], v[6:7], v[204:205]
	s_waitcnt lgkmcnt(0)
	v_pk_mul_f32 v[2:3], v[2:3], v[208:209]
	v_pk_mul_f32 v[0:1], v[0:1], v[206:207]
	v_pk_mul_f32 v[60:61], v[60:61], v[152:153]
	v_pk_mul_f32 v[56:57], v[56:57], v[156:157]
	v_pk_mul_f32 v[52:53], v[52:53], v[202:203]
	v_pk_mul_f32 v[62:63], v[62:63], v[154:155]
	v_pk_mul_f32 v[58:59], v[58:59], v[158:159]
	v_pk_mul_f32 v[54:55], v[54:55], v[204:205]
	v_pk_mul_f32 v[50:51], v[50:51], v[208:209]
	v_pk_mul_f32 v[48:49], v[48:49], v[206:207]
	v_pk_mul_f32 v[44:45], v[44:45], v[152:153]
	v_pk_mul_f32 v[40:41], v[40:41], v[156:157]
	v_pk_mul_f32 v[36:37], v[36:37], v[202:203]
	v_pk_mul_f32 v[46:47], v[46:47], v[154:155]
	v_pk_mul_f32 v[42:43], v[42:43], v[158:159]
	v_pk_mul_f32 v[38:39], v[38:39], v[204:205]
	v_pk_mul_f32 v[34:35], v[34:35], v[208:209]
	v_pk_mul_f32 v[32:33], v[32:33], v[206:207]
	v_pk_mul_f32 v[28:29], v[28:29], v[152:153]
	v_pk_mul_f32 v[24:25], v[24:25], v[156:157]
	v_pk_mul_f32 v[20:21], v[20:21], v[202:203]
	v_pk_mul_f32 v[30:31], v[30:31], v[154:155]
	v_pk_mul_f32 v[26:27], v[26:27], v[158:159]
	v_pk_mul_f32 v[22:23], v[22:23], v[204:205]
	v_pk_mul_f32 v[18:19], v[18:19], v[208:209]
	v_pk_mul_f32 v[16:17], v[16:17], v[206:207]

; #define SBAR() __builtin_amdgcn_sched_barrier(0)
; __device__ __forceinline__ void partialSM(f32x16& p0, f32x16& p1, float& m_reg, float& mn, float& alpha) {
;     ...
;   float pmax = p0[0]; for (int r = 1; r < 16; ++r) pmax = fmaxf(pmax, p0[r]); for (int r = 0; r < 16; ++r) pmax = fmaxf(pmax, p1[r]);
;   { auto rr = __builtin_amdgcn_permlane32_swap(__float_as_uint(pmax), __float_as_uint(pmax), false, false);
;     pmax = fmaxf(__uint_as_float(rr[0]), __uint_as_float(rr[1])); }
;   if (__builtin_expect(__all(pmax - m_reg <= THR / SCALE), 1)) { mn = m_reg; alpha = 1.f; }
;   else { mn = fmaxf(m_reg, pmax); alpha = __builtin_amdgcn_exp2f((m_reg - mn) * C); m_reg = mn; }
; template <int D0> __device__ __forceinline__ void pv_one(f32x16& od, int vb, bf16x8 pa0, bf16x8 pa1, bf16x8 pa2, bf16x8 pa3) {
;   const s16x4 l0 = tr_read<v_rd_off(D0, 0, 0)>(vb), h0 = tr_read<v_rd_off(D0, 0, 1)>(vb), l1 = tr_read<v_rd_off(D0, 1, 0)>(vb), h1 = tr_read<v_rd_off(D0, 1, 1)>(vb);
;   const s16x4 l2 = tr_read<v_rd_off(D0, 2, 0)>(vb), h2 = tr_read<v_rd_off(D0, 2, 1)>(vb), l3 = tr_read<v_rd_off(D0, 3, 0)>(vb), h3 = tr_read<v_rd_off(D0, 3, 1)>(vb);
;   asm volatile("s_waitcnt lgkmcnt(0)" ::: "memory"); SBAR();
;     ...
;   od = __builtin_amdgcn_mfma_f32_32x32x16_bf16(pa0, PK(l0, h0), od, 0, 0, 0);
;   od = __builtin_amdgcn_mfma_f32_32x32x16_bf16(pa1, PK(l1, h1), od, 0, 0, 0);
;   od = __builtin_amdgcn_mfma_f32_32x32x16_bf16(pa2, PK(l2, h2), od, 0, 0, 0);
;   od = __builtin_amdgcn_mfma_f32_32x32x16_bf16(pa3, PK(l3, h3), od, 0, 0, 0);
;     ...
; }
; __device__ __forceinline__ void pv_d0(f32x16* o, int vb, bf16x8 pa0, bf16x8 pa1, bf16x8 pa2, bf16x8 pa3) {
;   pv_one<0>(o[0], vb, pa0, pa1, pa2, pa3); pv_one<1>(o[1], vb, pa0, pa1, pa2, pa3); pv_one<2>(o[2], vb, pa0, pa1, pa2, pa3); pv_one<3>(o[3], vb, pa0, pa1, pa2, pa3);
.LBB0_460:
	ds_read_b64_tr_b16 v[170:171], v186 offset:0
	ds_read_b64_tr_b16 v[172:173], v186 offset:0x800
	ds_read_b64_tr_b16 v[174:175], v186 offset:0x1000
	ds_read_b64_tr_b16 v[176:177], v186 offset:0x1800
	ds_read_b64_tr_b16 v[204:205], v186 offset:0x2000
	ds_read_b64_tr_b16 v[206:207], v186 offset:0x2800
	ds_read_b64_tr_b16 v[208:209], v186 offset:0x3000
	ds_read_b64_tr_b16 v[210:211], v186 offset:0x3800
	s_nop 0
	s_waitcnt lgkmcnt(6)
	v_mfma_f32_32x32x16_bf16 v[0:15], v[146:149], v[170:173], v[0:15]
	ds_read_b64_tr_b16 v[170:171], v186 offset:0x200
	ds_read_b64_tr_b16 v[172:173], v186 offset:0xa00
	s_waitcnt lgkmcnt(6)
	v_mfma_f32_32x32x16_bf16 v[0:15], v[150:153], v[174:177], v[0:15]
	ds_read_b64_tr_b16 v[174:175], v186 offset:0x1200
	ds_read_b64_tr_b16 v[176:177], v186 offset:0x1a00
	s_waitcnt lgkmcnt(6)
	v_mfma_f32_32x32x16_bf16 v[0:15], v[154:157], v[204:207], v[0:15]
	ds_read_b64_tr_b16 v[204:205], v186 offset:0x2200
	ds_read_b64_tr_b16 v[206:207], v186 offset:0x2a00
	s_waitcnt lgkmcnt(6)
	v_mfma_f32_32x32x16_bf16 v[0:15], v[158:161], v[208:211], v[0:15]
	ds_read_b64_tr_b16 v[208:209], v186 offset:0x3200
	ds_read_b64_tr_b16 v[210:211], v186 offset:0x3a00
	s_waitcnt lgkmcnt(6)
	v_mfma_f32_32x32x16_bf16 v[48:63], v[146:149], v[170:173], v[48:63]
	ds_read_b64_tr_b16 v[170:171], v186 offset:0x400
	ds_read_b64_tr_b16 v[172:173], v186 offset:0xc00
	s_waitcnt lgkmcnt(6)
	v_mfma_f32_32x32x16_bf16 v[48:63], v[150:153], v[174:177], v[48:63]
	ds_read_b64_tr_b16 v[174:175], v186 offset:0x1400
	ds_read_b64_tr_b16 v[176:177], v186 offset:0x1c00
	s_waitcnt lgkmcnt(6)
	v_mfma_f32_32x32x16_bf16 v[48:63], v[154:157], v[204:207], v[48:63]
	ds_read_b64_tr_b16 v[204:205], v186 offset:0x2400
	ds_read_b64_tr_b16 v[206:207], v186 offset:0x2c00
	s_waitcnt lgkmcnt(6)
	v_mfma_f32_32x32x16_bf16 v[48:63], v[158:161], v[208:211], v[48:63]
	ds_read_b64_tr_b16 v[208:209], v186 offset:0x3400
	ds_read_b64_tr_b16 v[210:211], v186 offset:0x3c00
	s_waitcnt lgkmcnt(6)
	v_mfma_f32_32x32x16_bf16 v[32:47], v[146:149], v[170:173], v[32:47]
	ds_read_b64_tr_b16 v[170:171], v186 offset:0x600
	ds_read_b64_tr_b16 v[172:173], v186 offset:0xe00
	s_waitcnt lgkmcnt(6)
	v_mfma_f32_32x32x16_bf16 v[32:47], v[150:153], v[174:177], v[32:47]
	ds_read_b64_tr_b16 v[174:175], v186 offset:0x1600
	ds_read_b64_tr_b16 v[176:177], v186 offset:0x1e00
	s_waitcnt lgkmcnt(6)
	v_mfma_f32_32x32x16_bf16 v[32:47], v[154:157], v[204:207], v[32:47]
	ds_read_b64_tr_b16 v[204:205], v186 offset:0x2600
	ds_read_b64_tr_b16 v[206:207], v186 offset:0x2e00
	s_waitcnt lgkmcnt(6)
	v_mfma_f32_32x32x16_bf16 v[32:47], v[158:161], v[208:211], v[32:47]
	ds_read_b64_tr_b16 v[208:209], v186 offset:0x3600
	ds_read_b64_tr_b16 v[210:211], v186 offset:0x3e00
	s_waitcnt lgkmcnt(6)
	v_mfma_f32_32x32x16_bf16 v[16:31], v[146:149], v[170:173], v[16:31]
	v_max_f32_e32 v146, v81, v81
	v_max_f32_e32 v147, v80, v80
	v_max_f32_e32 v146, v147, v146
	v_max3_f32 v146, v146, v82, v83
	v_max3_f32 v146, v146, v84, v85
	v_max3_f32 v146, v146, v86, v87
	v_max3_f32 v146, v146, v88, v89
	v_max3_f32 v146, v146, v90, v91
	v_max3_f32 v146, v146, v92, v93
	s_waitcnt lgkmcnt(4)
	v_mfma_f32_32x32x16_bf16 v[16:31], v[150:153], v[174:177], v[16:31]
	v_max3_f32 v146, v146, v94, v95
	v_max3_f32 v146, v146, v64, v65
	v_max3_f32 v146, v146, v66, v67
	v_max3_f32 v146, v146, v68, v69
	v_max3_f32 v146, v146, v70, v71
	v_max3_f32 v146, v146, v72, v73
	v_max3_f32 v146, v146, v74, v75
	v_max3_f32 v146, v146, v76, v77
	s_waitcnt lgkmcnt(2)
	v_mfma_f32_32x32x16_bf16 v[16:31], v[154:157], v[204:207], v[16:31]
	v_max3_f32 v146, v146, v78, v79
	v_mov_b32_e32 v147, v146
	s_nop 1
	v_permlane32_swap_b32_e32 v146, v147
	v_max_f32_e32 v147, v147, v147
	v_max_f32_e32 v146, v146, v146
	v_max_f32_e32 v146, v146, v147
	v_sub_f32_e32 v147, v146, v201
	v_cmp_ge_f32_e32 vcc, s87, v147
	v_max_f32_e32 v147, v201, v201
	v_max_f32_e32 v147, v147, v146
	s_waitcnt lgkmcnt(0)
	v_mfma_f32_32x32x16_bf16 v[16:31], v[158:161], v[208:211], v[16:31]
	v_sub_f32_e32 v146, v201, v147
	v_mul_f32_e32 v146, 0x3e0293ee, v146
	v_exp_f32_e32 v146, v146
	s_cmp_eq_u64 vcc, exec
	s_cselect_b64 s[42:43], -1, 0
	s_waitcnt vmcnt(0)
	s_barrier
	s_add_i32 m0, s52, 0x0
	s_nop 0
	global_load_lds_dwordx4 v232, s[48:49]
	s_add_i32 m0, s52, 0x400
	s_nop 0
	global_load_lds_dwordx4 v233, s[48:49]
	s_add_i32 m0, s53, 0x4000
	s_nop 0
	global_load_lds_dwordx4 v234, s[50:51]
	s_add_i32 m0, s53, 0x4400
	s_nop 0
	global_load_lds_dwordx4 v235, s[50:51]
	s_add_u32 s48, s48, 0x18000
	s_addc_u32 s49, s49, 0
	s_add_u32 s50, s50, 0xc0000
	s_addc_u32 s51, s51, 0
	v_cndmask_b32_e64 v146, v146, 1.0, s[42:43]
	v_cmp_gt_f32_e32 vcc, 1.0, v146
	s_cbranch_vccz .LBB0_464
	s_and_saveexec_b64 s[6:7], s[40:41]
	ds_write_b32 v184, v146 offset:128
	s_or_b64 exec, exec, s[6:7]
	s_waitcnt lgkmcnt(0)
	v_add_u32_e32 v142, v183, v96
	ds_read_b128 v[130:133], v142 offset:224
	ds_read_b128 v[134:137], v142 offset:192
	ds_read_b128 v[138:141], v142 offset:160
	ds_read_b128 v[142:145], v142 offset:128
	s_waitcnt lgkmcnt(3)
	v_pk_mul_f32 v[12:13], v[12:13], v[130:131]
	s_waitcnt lgkmcnt(2)
	v_pk_mul_f32 v[8:9], v[8:9], v[134:135]
	s_waitcnt lgkmcnt(1)
	v_pk_mul_f32 v[4:5], v[4:5], v[138:139]
	v_pk_mul_f32 v[14:15], v[14:15], v[132:133]
	v_pk_mul_f32 v[10:11], v[10:11], v[136:137]
	v_pk_mul_f32 v[6:7], v[6:7], v[140:141]
	s_waitcnt lgkmcnt(0)
	v_pk_mul_f32 v[2:3], v[2:3], v[144:145]
	v_pk_mul_f32 v[0:1], v[0:1], v[142:143]
	v_pk_mul_f32 v[60:61], v[60:61], v[130:131]
	v_pk_mul_f32 v[56:57], v[56:57], v[134:135]
	v_pk_mul_f32 v[52:53], v[52:53], v[138:139]
	v_pk_mul_f32 v[62:63], v[62:63], v[132:133]
	v_pk_mul_f32 v[58:59], v[58:59], v[136:137]
	v_pk_mul_f32 v[54:55], v[54:55], v[140:141]
	v_pk_mul_f32 v[50:51], v[50:51], v[144:145]
	v_pk_mul_f32 v[48:49], v[48:49], v[142:143]
	v_pk_mul_f32 v[44:45], v[44:45], v[130:131]
	v_pk_mul_f32 v[40:41], v[40:41], v[134:135]
	v_pk_mul_f32 v[36:37], v[36:37], v[138:139]
	v_pk_mul_f32 v[46:47], v[46:47], v[132:133]
	v_pk_mul_f32 v[42:43], v[42:43], v[136:137]
	v_pk_mul_f32 v[38:39], v[38:39], v[140:141]
	v_pk_mul_f32 v[34:35], v[34:35], v[144:145]
	v_pk_mul_f32 v[32:33], v[32:33], v[142:143]
	v_pk_mul_f32 v[28:29], v[28:29], v[130:131]
	v_pk_mul_f32 v[24:25], v[24:25], v[134:135]
	v_pk_mul_f32 v[20:21], v[20:21], v[138:139]
	v_pk_mul_f32 v[30:31], v[30:31], v[132:133]
	v_pk_mul_f32 v[26:27], v[26:27], v[136:137]
	v_pk_mul_f32 v[22:23], v[22:23], v[140:141]
	v_pk_mul_f32 v[18:19], v[18:19], v[144:145]
	v_pk_mul_f32 v[16:17], v[16:17], v[142:143]
